# DSA token loop: one static s_setprio 1 for waves 4-7 for the whole phase (reset at its end)
# speedup vs baseline: 1.0061x; 1.0061x over previous
.LBB0_516:
	s_cmp_lt_i32 s44, 5
	s_cselect_b64 s[2:3], -1, 0
	s_add_u32 s70, s54, 0x20c00000
	s_addc_u32 s71, s55, 0
	s_add_u32 s4, s54, 0x1800000
	s_addc_u32 s5, s55, 0
	s_and_b64 s[20:21], s[2:3], s[0:1]
	v_writelane_b32 v242, s4, 39
	s_andn2_b64 vcc, exec, s[20:21]
	s_nop 0
	v_writelane_b32 v242, s5, 40
	s_cbranch_vccnz .LBB0_1160
	s_lshl_b32 s0, s77, 3
	s_add_i32 s22, s76, s0
	s_lshl_b32 s40, s97, 3
	s_cmpk_lt_i32 s22, 0x2000
	v_mbcnt_hi_u32_b32 v1, -1, v175
	s_cselect_b64 s[0:1], -1, 0
	s_mov_b32 s91, 0
	s_waitcnt vmcnt(1)
	v_mov_b32_e32 v78, v1
	s_movk_i32 s41, 0x2000
	v_writelane_b32 v242, s0, 41
	s_cmpk_gt_i32 s22, 0x1fff
	v_and_b32_e32 v159, 64, v1
	v_xor_b32_e32 v155, 16, v1
	v_xor_b32_e32 v154, 32, v1
	v_xor_b32_e32 v160, 1, v1
	v_xor_b32_e32 v158, 2, v1
	v_xor_b32_e32 v157, 4, v1
	v_xor_b32_e32 v156, 8, v1
	v_writelane_b32 v242, s1, 42
	s_cbranch_scc1 .LBB0_1141
	v_writelane_b32 v242, s20, 43
	s_mul_i32 s0, s76, 0x2800
	s_add_i32 s89, s0, 0
	v_writelane_b32 v242, s21, 44
	v_writelane_b32 v242, s96, 45
	v_writelane_b32 v242, s78, 46
	v_add_u32_e32 v2, 64, v159
	s_mov_b32 s0, s22
	v_writelane_b32 v242, s79, 47
	v_writelane_b32 v242, s77, 48
	v_writelane_b32 v242, s76, 49
	v_writelane_b32 v242, s97, 50
	v_cmp_lt_i32_e32 vcc, v155, v2
	v_writelane_b32 v242, s0, 51
	s_lshl_b32 s12, s97, 4
	v_cndmask_b32_e32 v3, v1, v155, vcc
	v_cmp_lt_i32_e32 vcc, v154, v2
	v_writelane_b32 v242, s1, 52
	v_lshlrev_b32_e32 v161, 2, v3
	v_cndmask_b32_e32 v3, v1, v154, vcc
	v_cmp_lt_i32_e32 vcc, v160, v2
	v_writelane_b32 v242, s82, 53
	v_lshlrev_b32_e32 v162, 2, v3
	v_cndmask_b32_e32 v3, v1, v160, vcc
	v_cmp_lt_i32_e32 vcc, v158, v2
	v_writelane_b32 v242, s83, 54
	v_lshlrev_b32_e32 v163, 2, v3
	v_cndmask_b32_e32 v3, v1, v158, vcc
	v_cmp_lt_i32_e32 vcc, v157, v2
	v_writelane_b32 v242, s84, 55
	v_lshlrev_b32_e32 v164, 2, v3
	v_cndmask_b32_e32 v3, v1, v157, vcc
	v_cmp_lt_i32_e32 vcc, v156, v2
	v_writelane_b32 v242, s85, 56
	v_writelane_b32 v242, s86, 57
	v_cndmask_b32_e32 v2, v1, v156, vcc
	v_lshlrev_b32_e32 v165, 2, v3
	v_lshlrev_b32_e32 v166, 2, v2
	s_movk_i32 s33, 0x1000
	s_movk_i32 s56, 0x3000
	s_mov_b32 s64, 0x7060302
	s_mov_b32 s65, 0x10001
	v_mov_b32_e32 v147, 0
	v_mov_b32_e32 v167, 0x10001
	s_mov_b32 s34, 0x5040100
	s_movk_i32 s35, 0x3400
	s_mov_b64 s[94:95], 0x2800
	s_mov_b32 s13, 0x42fe0000
	s_mov_b32 s57, 0x40c0c00
	s_mov_b32 s88, 0xf800000
	v_mov_b32_e32 v168, 0x260
	v_bfrev_b32_e32 v169, 1
	v_mov_b32_e32 v170, 0xff800000
	v_mov_b32_e32 v171, 0x80
	s_mov_b32 s42, s22
	s_mov_b32 s14, 0
	s_mov_b32 s43, s22
	v_writelane_b32 v242, s87, 58
	v_writelane_b32 v242, s12, 59
	s_cmp_ge_u32 s76, 4
	s_cbranch_scc0 .Lprio_p4
	s_setprio 1
.Lprio_p4:
	s_branch .LBB0_520
.LBB0_519:
	s_add_i32 s43, s43, s40
	s_add_i32 s42, s42, s12
	s_cmpk_gt_i32 s43, 0x1fff
	s_cbranch_scc1 .LBB0_1140

.LBB0_1140:
	s_setprio 0
	v_readlane_b32 s78, v242, 46
	v_readlane_b32 s44, v242, 0
	v_readlane_b32 s60, v242, 7
	v_readlane_b32 s20, v242, 43
	v_readlane_b32 s77, v242, 48
	v_readlane_b32 s97, v242, 50
	v_readlane_b32 s79, v242, 47
	v_readlane_b32 s76, v242, 49
	v_readlane_b32 s45, v242, 1
	v_readlane_b32 s96, v242, 45
	v_readlane_b32 s61, v242, 8
	v_readlane_b32 s21, v242, 44
	v_readlane_b32 s22, v242, 51
	v_readlane_b32 s23, v242, 52
